# p7 modulation-vector loads issued together; p0 adaLN GEMV weight rows fetched one k-step ahead
# speedup vs baseline: 1.0275x; 1.0049x over previous
; #define LAS __attribute__((address_space(3)))
; __device__ __forceinline__ void p0_prologue(const Frame& F) {
;     ...
;         for (int it = F.blk; it < DEPTH * 96; it += F.G) {
;             const int l = it / 96, cb = it % 96, col = cb * 64 + lane;
;             const float* wm = wmod + (size_t)l * D * 6144 + (size_t)(128 * wave) * 6144 + col;
;             float acc[17];
; #pragma unroll
;             for (int r = 0; r < 17; ++r) acc[r] = 0.f;
;             for (int k = 0; k < 128; k += 8) {
;                 float w[8];
; #pragma unroll
;                 for (int q = 0; q < 8; ++q) w[q] = wm[(size_t)(k + q) * 6144];
; #pragma unroll
;                 for (int r = 0; r < 17; ++r) { const f32x4 s0 = *(LAS const f32x4*)(S + r * 1024 + 128 * wave + k), s1 = *(LAS const f32x4*)(S + r * 1024 + 128 * wave + k + 4);
;                     acc[r] += s0[0] * w[0] + s0[1] * w[1] + s0[2] * w[2] + s0[3] * w[3] + s1[0] * w[4] + s1[1] * w[5] + s1[2] * w[6] + s1[3] * w[7]; }
;             }
.LBB0_12:
	s_mul_hi_i32 s4, s30, 0x2aaaaaab
	s_lshr_b32 s5, s4, 31
	s_ashr_i32 s4, s4, 4
	s_add_i32 s9, s4, s5
	s_mul_i32 s4, s9, 0x60
	s_sub_i32 s4, s30, s4
	s_lshl_b32 s8, s4, 6
	s_mul_i32 s4, s9, 0x1800000
	v_add_u32_e32 v6, s8, v38
	s_mul_hi_i32 s5, s9, 0x1800000
	s_add_u32 s4, s17, s4
	v_ashrrev_i32_e32 v7, 31, v6
	s_addc_u32 s5, s18, s5
	v_lshl_add_u64 v[6:7], v[6:7], 2, s[4:5]
	s_mov_b32 s10, -8
	s_mov_b32 s11, s16
	v_mov_b32_e32 v8, 0
	v_mov_b32_e32 v9, v3
	v_mov_b32_e32 v10, 0
	v_mov_b32_e32 v11, v3
	v_mov_b32_e32 v12, 0
	v_mov_b32_e32 v13, v3
	v_mov_b32_e32 v14, 0
	v_mov_b32_e32 v15, v3
	v_mov_b32_e32 v16, 0
	v_mov_b32_e32 v17, v3
	v_mov_b32_e32 v18, 0
	v_mov_b32_e32 v19, v3
	v_mov_b32_e32 v20, 0
	v_mov_b32_e32 v21, v3
	v_mov_b32_e32 v22, 0
	v_mov_b32_e32 v23, v3
	v_mov_b32_e32 v41, 0
	v_add_co_u32_e64 v24, s[4:5], s19, v6
	global_load_dword v182, v[6:7], off
	s_nop 1
	v_addc_co_u32_e64 v25, s[4:5], -1, v7, s[4:5]
	v_add_co_u32_e64 v26, s[4:5], s20, v6
	s_nop 1
	v_addc_co_u32_e64 v27, s[4:5], -1, v7, s[4:5]
	v_add_co_u32_e64 v28, s[4:5], s21, v6
	s_nop 1
	v_addc_co_u32_e64 v29, s[4:5], -1, v7, s[4:5]
	v_add_co_u32_e64 v30, s[4:5], s22, v6
	s_nop 1
	v_addc_co_u32_e64 v31, s[4:5], -1, v7, s[4:5]
	v_add_co_u32_e64 v32, s[4:5], s23, v6
	s_nop 1
	v_addc_co_u32_e64 v33, s[4:5], -1, v7, s[4:5]
	v_add_co_u32_e64 v34, s[4:5], s27, v6
	s_nop 1
	v_addc_co_u32_e64 v35, s[4:5], -1, v7, s[4:5]
	v_add_co_u32_e64 v36, s[4:5], s28, v6
	s_nop 1
	v_addc_co_u32_e64 v37, s[4:5], -1, v7, s[4:5]
	global_load_dword v183, v[24:25], off
	global_load_dword v184, v[26:27], off
	global_load_dword v185, v[28:29], off
	global_load_dword v186, v[30:31], off
	global_load_dword v187, v[32:33], off
	global_load_dword v188, v[34:35], off
	global_load_dword v189, v[36:37], off
.LBB0_13:
	s_waitcnt vmcnt(0)
	v_mov_b32_e32 v2, v182
	v_mov_b32_e32 v168, v183
	v_mov_b32_e32 v170, v184
	v_mov_b32_e32 v172, v185
	v_mov_b32_e32 v174, v186
	v_mov_b32_e32 v176, v187
	v_mov_b32_e32 v178, v188
	v_mov_b32_e32 v180, v189
	v_lshl_add_u64 v[6:7], v[6:7], 0, s[6:7]
	v_mov_b32_e32 v42, s11
	s_add_i32 s10, s10, 8
	s_cmpk_gt_u32 s10, 0x77
	s_cbranch_scc1 .Lp0_nopf
	v_add_co_u32_e64 v24, s[4:5], s19, v6
	global_load_dword v182, v[6:7], off
	s_nop 1
	v_addc_co_u32_e64 v25, s[4:5], -1, v7, s[4:5]
	v_add_co_u32_e64 v26, s[4:5], s20, v6
	s_nop 1
	v_addc_co_u32_e64 v27, s[4:5], -1, v7, s[4:5]
	v_add_co_u32_e64 v28, s[4:5], s21, v6
	s_nop 1
	v_addc_co_u32_e64 v29, s[4:5], -1, v7, s[4:5]
	v_add_co_u32_e64 v30, s[4:5], s22, v6
	s_nop 1
	v_addc_co_u32_e64 v31, s[4:5], -1, v7, s[4:5]
	v_add_co_u32_e64 v32, s[4:5], s23, v6
	s_nop 1
	v_addc_co_u32_e64 v33, s[4:5], -1, v7, s[4:5]
	v_add_co_u32_e64 v34, s[4:5], s27, v6
	s_nop 1
	v_addc_co_u32_e64 v35, s[4:5], -1, v7, s[4:5]
	v_add_co_u32_e64 v36, s[4:5], s28, v6
	s_nop 1
	v_addc_co_u32_e64 v37, s[4:5], -1, v7, s[4:5]
	global_load_dword v183, v[24:25], off
	global_load_dword v184, v[26:27], off
	global_load_dword v185, v[28:29], off
	global_load_dword v186, v[30:31], off
	global_load_dword v187, v[32:33], off
	global_load_dword v188, v[34:35], off
	global_load_dword v189, v[36:37], off
.Lp0_nopf:
	ds_read_b128 v[24:27], v42
	ds_read_b128 v[28:31], v42 offset:16
	ds_read_b128 v[32:35], v42 offset:4096
	ds_read_b128 v[44:47], v42 offset:4112
	ds_read_b128 v[48:51], v42 offset:8192
	ds_read_b128 v[52:55], v42 offset:8208
	ds_read_b128 v[56:59], v42 offset:12288
	ds_read_b128 v[60:63], v42 offset:12304
	ds_read_b128 v[64:67], v42 offset:16384
	ds_read_b128 v[68:71], v42 offset:16400
	ds_read_b128 v[72:75], v42 offset:20480
	ds_read_b128 v[76:79], v42 offset:20496
	ds_read_b128 v[80:83], v42 offset:24576
	ds_read_b128 v[84:87], v42 offset:24592
	ds_read_b128 v[88:91], v42 offset:28672
	ds_read_b128 v[92:95], v42 offset:28688
	ds_read_b128 v[96:99], v42 offset:32768
	ds_read_b128 v[100:103], v42 offset:32784
	ds_read_b128 v[104:107], v42 offset:36864
	ds_read_b128 v[108:111], v42 offset:36880
	ds_read_b128 v[112:115], v42 offset:40960
	ds_read_b128 v[116:119], v42 offset:40976
	ds_read_b128 v[120:123], v42 offset:45056
	ds_read_b128 v[124:127], v42 offset:45072
	ds_read_b128 v[128:131], v42 offset:49152
	ds_read_b128 v[132:135], v42 offset:49168
	ds_read_b128 v[136:139], v42 offset:53248
	ds_read_b128 v[140:143], v42 offset:53264
	ds_read_b128 v[144:147], v42 offset:57344
	ds_read_b128 v[148:151], v42 offset:57360
	ds_read_b128 v[152:155], v42 offset:61440
	ds_read_b128 v[156:159], v42 offset:61456
	s_add_i32 s4, s11, 0x10000
	s_add_i32 s5, s11, 0x10010
	v_mov_b32_e32 v36, s4
	v_mov_b32_e32 v37, s5
	ds_read_b128 v[160:163], v36
	ds_read_b128 v[164:167], v37
	s_waitcnt lgkmcnt(14)
	v_mov_b32_e32 v37, v32
	v_mov_b32_e32 v32, v25
	v_mov_b32_e32 v25, v34
	v_mov_b32_e32 v34, v27
	v_mov_b32_e32 v27, v44
	v_mov_b32_e32 v44, v29
	v_mov_b32_e32 v29, v46
	v_mov_b32_e32 v46, v31
	v_mov_b32_e32 v31, v56
	v_mov_b32_e32 v56, v49
	v_mov_b32_e32 v49, v60
	v_mov_b32_e32 v60, v53
	v_mov_b32_e32 v53, v72
	v_mov_b32_e32 v72, v65
	v_mov_b32_e32 v65, v76
	v_mov_b32_e32 v76, v69
	v_mov_b32_e32 v69, v88
	v_mov_b32_e32 v88, v81
	v_mov_b32_e32 v81, v92
	v_mov_b32_e32 v92, v85
	v_mov_b32_e32 v85, v104
	v_mov_b32_e32 v104, v97
	v_mov_b32_e32 v97, v108
	v_mov_b32_e32 v108, v101
	s_waitcnt lgkmcnt(11)
	v_mov_b32_e32 v101, v120
	v_mov_b32_e32 v120, v113
	s_waitcnt lgkmcnt(10)
	v_mov_b32_e32 v113, v124
	v_mov_b32_e32 v124, v117
	s_waitcnt lgkmcnt(7)
	v_mov_b32_e32 v117, v136
	v_mov_b32_e32 v136, v129
	s_waitcnt lgkmcnt(6)
	v_mov_b32_e32 v129, v140
	v_mov_b32_e32 v140, v133
	s_waitcnt lgkmcnt(3)
; #define LAS __attribute__((address_space(3)))
; __device__ __forceinline__ void p0_prologue(const Frame& F) {
;     ...
;             for (int k = 0; k < 128; k += 8) {
;                 float w[8];
; #pragma unroll
;                 for (int q = 0; q < 8; ++q) w[q] = wm[(size_t)(k + q) * 6144];
; #pragma unroll
;                 for (int r = 0; r < 17; ++r) { const f32x4 s0 = *(LAS const f32x4*)(S + r * 1024 + 128 * wave + k), s1 = *(LAS const f32x4*)(S + r * 1024 + 128 * wave + k + 4);
;                     acc[r] += s0[0] * w[0] + s0[1] * w[1] + s0[2] * w[2] + s0[3] * w[3] + s1[0] * w[4] + s1[1] * w[5] + s1[2] * w[6] + s1[3] * w[7]; }
;             }
	v_mov_b32_e32 v133, v152
	v_mov_b32_e32 v152, v145
	v_mov_b32_e32 v36, v24
	v_mov_b32_e32 v24, v26
	v_mov_b32_e32 v26, v28
	v_mov_b32_e32 v28, v30
	v_mov_b32_e32 v30, v48
	v_mov_b32_e32 v48, v52
	v_mov_b32_e32 v52, v64
	v_mov_b32_e32 v64, v68
	v_mov_b32_e32 v68, v80
	v_mov_b32_e32 v80, v84
	v_mov_b32_e32 v84, v96
	v_mov_b32_e32 v96, v100
	v_mov_b32_e32 v100, v112
	v_mov_b32_e32 v112, v116
	v_mov_b32_e32 v116, v128
	v_mov_b32_e32 v128, v132
	v_mov_b32_e32 v132, v144
	v_mov_b32_e32 v144, v148
	s_waitcnt lgkmcnt(2)
	v_mov_b32_e32 v145, v156
	v_mov_b32_e32 v156, v149
	v_mov_b32_e32 v42, v50
	v_mov_b32_e32 v43, v58
	v_mov_b32_e32 v58, v51
	v_mov_b32_e32 v50, v54
	v_mov_b32_e32 v51, v62
	v_mov_b32_e32 v62, v55
	v_mov_b32_e32 v54, v66
	v_mov_b32_e32 v55, v74
	v_mov_b32_e32 v74, v67
	v_mov_b32_e32 v66, v70
	v_mov_b32_e32 v67, v78
	v_mov_b32_e32 v78, v71
	v_mov_b32_e32 v70, v82
	v_mov_b32_e32 v71, v90
	v_pk_mul_f32 v[32:33], v[170:171], v[32:33] op_sel_hi:[0,1]
	v_pk_mul_f32 v[56:57], v[170:171], v[56:57] op_sel_hi:[0,1]
	v_pk_mul_f32 v[72:73], v[170:171], v[72:73] op_sel_hi:[0,1]
	v_pk_mul_f32 v[88:89], v[170:171], v[88:89] op_sel_hi:[0,1]
	v_pk_mul_f32 v[104:105], v[170:171], v[104:105] op_sel_hi:[0,1]
	v_pk_mul_f32 v[120:121], v[170:171], v[120:121] op_sel_hi:[0,1]
	v_pk_mul_f32 v[136:137], v[170:171], v[136:137] op_sel_hi:[0,1]
	v_pk_mul_f32 v[148:149], v[170:171], v[152:153] op_sel_hi:[0,1]
	v_mov_b32_e32 v90, v83
	v_mov_b32_e32 v82, v86
	v_mov_b32_e32 v83, v94
	v_mov_b32_e32 v94, v87
	v_mov_b32_e32 v86, v98
	v_mov_b32_e32 v87, v106
	v_mov_b32_e32 v106, v99
	v_mov_b32_e32 v98, v102
	v_mov_b32_e32 v99, v110
	v_mov_b32_e32 v110, v103
	v_mov_b32_e32 v102, v114
	v_mov_b32_e32 v103, v122
	v_mov_b32_e32 v122, v115
	v_mov_b32_e32 v114, v118
	v_mov_b32_e32 v115, v126
	v_mov_b32_e32 v126, v119
	v_mov_b32_e32 v118, v130
	v_mov_b32_e32 v119, v138
	v_mov_b32_e32 v138, v131
	v_mov_b32_e32 v130, v134
	v_mov_b32_e32 v131, v142
	v_mov_b32_e32 v142, v135
	v_mov_b32_e32 v134, v146
	v_mov_b32_e32 v135, v154
	v_pk_fma_f32 v[32:33], v[168:169], v[36:37], v[32:33] op_sel_hi:[0,1,1]
	v_pk_fma_f32 v[30:31], v[168:169], v[30:31], v[56:57] op_sel_hi:[0,1,1]
	v_pk_fma_f32 v[36:37], v[168:169], v[52:53], v[72:73] op_sel_hi:[0,1,1]
	v_pk_fma_f32 v[52:53], v[168:169], v[68:69], v[88:89] op_sel_hi:[0,1,1]
	v_pk_fma_f32 v[56:57], v[168:169], v[84:85], v[104:105] op_sel_hi:[0,1,1]
	v_pk_fma_f32 v[68:69], v[168:169], v[100:101], v[120:121] op_sel_hi:[0,1,1]
	v_pk_fma_f32 v[72:73], v[168:169], v[116:117], v[136:137] op_sel_hi:[0,1,1]
	v_pk_fma_f32 v[84:85], v[168:169], v[132:133], v[148:149] op_sel_hi:[0,1,1]
	v_mov_b32_e32 v169, v170
	v_mov_b32_e32 v154, v147
	v_pk_fma_f32 v[24:25], v[172:173], v[24:25], v[32:33] op_sel_hi:[0,1,1]
	v_pk_fma_f32 v[30:31], v[172:173], v[42:43], v[30:31] op_sel_hi:[0,1,1]
	v_pk_fma_f32 v[32:33], v[172:173], v[54:55], v[36:37] op_sel_hi:[0,1,1]
	v_pk_fma_f32 v[36:37], v[172:173], v[70:71], v[52:53] op_sel_hi:[0,1,1]
	v_pk_fma_f32 v[42:43], v[172:173], v[86:87], v[56:57] op_sel_hi:[0,1,1]
	v_pk_fma_f32 v[52:53], v[172:173], v[102:103], v[68:69] op_sel_hi:[0,1,1]
	v_pk_fma_f32 v[54:55], v[172:173], v[118:119], v[72:73] op_sel_hi:[0,1,1]
	v_pk_fma_f32 v[56:57], v[172:173], v[134:135], v[84:85] op_sel_hi:[0,1,1]
	s_waitcnt lgkmcnt(1)
; #define LAS __attribute__((address_space(3)))
; __device__ __forceinline__ void p0_prologue(const Frame& F) {
;     ...
;             for (int k = 0; k < 128; k += 8) {
;                 float w[8];
; #pragma unroll
;                 for (int q = 0; q < 8; ++q) w[q] = wm[(size_t)(k + q) * 6144];
; #pragma unroll
;                 for (int r = 0; r < 17; ++r) { const f32x4 s0 = *(LAS const f32x4*)(S + r * 1024 + 128 * wave + k), s1 = *(LAS const f32x4*)(S + r * 1024 + 128 * wave + k + 4);
;                     acc[r] += s0[0] * w[0] + s0[1] * w[1] + s0[2] * w[2] + s0[3] * w[3] + s1[0] * w[4] + s1[1] * w[5] + s1[2] * w[6] + s1[3] * w[7]; }
;             }
; #pragma unroll
;             for (int r = 0; r < 17; ++r) red[(wave * 17 + r) * 64 + lane] = acc[r];
;             __syncthreads();
;             for (int o = F.tid; o < 17 * 64; o += NTHREADS) { const int r = o >> 6, cc = o & 63; float a = 0.f;
; #pragma unroll
;                 for (int w = 0; w < 8; ++w) a += red[(w * 17 + r) * 64 + cc];
;                 modp[((size_t)l * 17 + r) * 6144 + cb * 64 + cc] = a + bmod[l * 6144 + cb * 64 + cc]; }
	v_pk_mul_f32 v[68:69], v[168:169], v[160:161]
	v_mov_b32_e32 v173, v174
	v_pk_fma_f32 v[24:25], v[174:175], v[34:35], v[24:25] op_sel_hi:[0,1,1]
	v_pk_fma_f32 v[30:31], v[174:175], v[58:59], v[30:31] op_sel_hi:[0,1,1]
	v_pk_fma_f32 v[32:33], v[174:175], v[74:75], v[32:33] op_sel_hi:[0,1,1]
	v_pk_fma_f32 v[34:35], v[174:175], v[90:91], v[36:37] op_sel_hi:[0,1,1]
	v_pk_fma_f32 v[36:37], v[174:175], v[106:107], v[42:43] op_sel_hi:[0,1,1]
	v_pk_fma_f32 v[42:43], v[174:175], v[122:123], v[52:53] op_sel_hi:[0,1,1]
	v_pk_fma_f32 v[52:53], v[174:175], v[138:139], v[54:55] op_sel_hi:[0,1,1]
	v_pk_fma_f32 v[54:55], v[174:175], v[154:155], v[56:57] op_sel_hi:[0,1,1]
	v_pk_mul_f32 v[56:57], v[172:173], v[162:163]
	v_add_f32_e32 v58, v68, v69
	v_pk_fma_f32 v[24:25], v[176:177], v[26:27], v[24:25] op_sel_hi:[0,1,1]
	v_pk_fma_f32 v[26:27], v[176:177], v[48:49], v[30:31] op_sel_hi:[0,1,1]
	v_pk_fma_f32 v[30:31], v[176:177], v[64:65], v[32:33] op_sel_hi:[0,1,1]
	v_pk_fma_f32 v[32:33], v[176:177], v[80:81], v[34:35] op_sel_hi:[0,1,1]
	v_pk_fma_f32 v[34:35], v[176:177], v[96:97], v[36:37] op_sel_hi:[0,1,1]
	v_pk_fma_f32 v[36:37], v[176:177], v[112:113], v[42:43] op_sel_hi:[0,1,1]
	v_pk_fma_f32 v[42:43], v[176:177], v[128:129], v[52:53] op_sel_hi:[0,1,1]
	v_pk_fma_f32 v[48:49], v[176:177], v[144:145], v[54:55] op_sel_hi:[0,1,1]
	v_mov_b32_e32 v177, v178
	v_add_f32_e32 v52, v56, v58
	v_mov_b32_e32 v146, v150
	v_mov_b32_e32 v147, v158
	v_pk_fma_f32 v[24:25], v[178:179], v[44:45], v[24:25] op_sel_hi:[0,1,1]
	v_pk_fma_f32 v[26:27], v[178:179], v[60:61], v[26:27] op_sel_hi:[0,1,1]
	v_pk_fma_f32 v[30:31], v[178:179], v[76:77], v[30:31] op_sel_hi:[0,1,1]
	v_pk_fma_f32 v[32:33], v[178:179], v[92:93], v[32:33] op_sel_hi:[0,1,1]
	v_pk_fma_f32 v[34:35], v[178:179], v[108:109], v[34:35] op_sel_hi:[0,1,1]
	v_pk_fma_f32 v[36:37], v[178:179], v[124:125], v[36:37] op_sel_hi:[0,1,1]
	v_pk_fma_f32 v[42:43], v[178:179], v[140:141], v[42:43] op_sel_hi:[0,1,1]
	v_pk_fma_f32 v[44:45], v[178:179], v[156:157], v[48:49] op_sel_hi:[0,1,1]
	s_waitcnt lgkmcnt(0)
	v_pk_mul_f32 v[48:49], v[176:177], v[164:165]
	v_add_f32_e32 v52, v57, v52
	v_mov_b32_e32 v158, v151
	v_pk_fma_f32 v[24:25], v[180:181], v[28:29], v[24:25] op_sel_hi:[0,1,1]
	v_pk_fma_f32 v[26:27], v[180:181], v[50:51], v[26:27] op_sel_hi:[0,1,1]
	v_pk_fma_f32 v[28:29], v[180:181], v[66:67], v[30:31] op_sel_hi:[0,1,1]
	v_pk_fma_f32 v[30:31], v[180:181], v[82:83], v[32:33] op_sel_hi:[0,1,1]
	v_pk_fma_f32 v[32:33], v[180:181], v[98:99], v[34:35] op_sel_hi:[0,1,1]
	v_pk_fma_f32 v[34:35], v[180:181], v[114:115], v[36:37] op_sel_hi:[0,1,1]
	v_pk_fma_f32 v[36:37], v[180:181], v[130:131], v[42:43] op_sel_hi:[0,1,1]
	v_pk_fma_f32 v[42:43], v[180:181], v[146:147], v[44:45] op_sel_hi:[0,1,1]
	v_mov_b32_e32 v181, v2
	v_add_f32_e32 v48, v48, v52
	v_pk_fma_f32 v[24:25], v[2:3], v[46:47], v[24:25] op_sel_hi:[0,1,1]
	v_pk_fma_f32 v[26:27], v[2:3], v[62:63], v[26:27] op_sel_hi:[0,1,1]
	v_pk_fma_f32 v[28:29], v[2:3], v[78:79], v[28:29] op_sel_hi:[0,1,1]
	v_pk_fma_f32 v[30:31], v[2:3], v[94:95], v[30:31] op_sel_hi:[0,1,1]
	v_pk_fma_f32 v[32:33], v[2:3], v[110:111], v[32:33] op_sel_hi:[0,1,1]
	v_pk_fma_f32 v[34:35], v[2:3], v[126:127], v[34:35] op_sel_hi:[0,1,1]
	v_pk_fma_f32 v[36:37], v[2:3], v[142:143], v[36:37] op_sel_hi:[0,1,1]
	v_pk_fma_f32 v[42:43], v[2:3], v[158:159], v[42:43] op_sel_hi:[0,1,1]
	v_pk_mul_f32 v[44:45], v[180:181], v[166:167]
	v_add_f32_e32 v2, v49, v48
	v_add_f32_e32 v2, v44, v2
	s_add_i32 s11, s11, 32
	v_add_f32_e32 v2, v45, v2
	s_cmpk_gt_u32 s10, 0x77
	v_pk_add_f32 v[8:9], v[8:9], v[24:25]
	v_pk_add_f32 v[10:11], v[10:11], v[26:27]
	v_pk_add_f32 v[12:13], v[12:13], v[28:29]
	v_pk_add_f32 v[14:15], v[14:15], v[30:31]
	v_pk_add_f32 v[16:17], v[16:17], v[32:33]
	v_pk_add_f32 v[18:19], v[18:19], v[34:35]
	v_pk_add_f32 v[20:21], v[20:21], v[36:37]
	v_pk_add_f32 v[22:23], v[22:23], v[42:43]
	v_add_f32_e32 v41, v41, v2
	s_cbranch_scc0 .LBB0_13
	ds_write2st64_b32 v40, v8, v9 offset1:1
	ds_write2st64_b32 v40, v10, v11 offset0:2 offset1:3
	ds_write2st64_b32 v40, v12, v13 offset0:4 offset1:5
	ds_write2st64_b32 v40, v14, v15 offset0:6 offset1:7
	ds_write2st64_b32 v40, v16, v17 offset0:8 offset1:9
	ds_write2st64_b32 v40, v18, v19 offset0:10 offset1:11
	ds_write2st64_b32 v40, v20, v21 offset0:12 offset1:13
	ds_write2st64_b32 v40, v22, v23 offset0:14 offset1:15
	ds_write_b32 v40, v41 offset:4096
	s_waitcnt lgkmcnt(0)
	s_barrier
	s_and_saveexec_b64 s[10:11], vcc
	s_cbranch_execz .LBB0_11
	s_mul_i32 s4, s9, 0x1800
	s_add_i32 s4, s4, s8
	v_or_b32_e32 v6, s4, v1
	s_mul_hi_i32 s13, s9, 17
	s_mul_i32 s12, s9, 17
	s_ashr_i32 s9, s8, 31
	v_ashrrev_i32_e32 v7, 31, v6
	v_lshl_add_u64 v[6:7], v[6:7], 2, s[2:3]
	v_lshl_add_u64 v[8:9], s[8:9], 2, v[4:5]
	s_mov_b64 s[8:9], 0
	v_mov_b32_e32 v2, v0

; __device__ __forceinline__ void p7_norm2(const Frame& F, int layer) {
;     ...
;         if (mR != cur_m) { cur_m = mR; const float* sh = modl + mR * 6144 + 3 * 1024; const float* sc = sh + 1024;
; #pragma unroll
;             for (int j = 0; j < 4; ++j) { const int k = 4 * (lane + 64 * j); W1[j] = *(const f32x4*)(n2w + k) * (*(const f32x4*)(sc + k) + 1.f); S0[j] = *(const f32x4*)(sh + k); } }
.LBB0_831:
	s_cmp_lt_i32 s2, s18
	s_cselect_b64 s[10:11], -1, 0
	s_and_b64 s[12:13], s[10:11], exec
	s_cselect_b32 s3, s2, 0
	s_min_i32 s12, s3, 0x8000
	s_ashr_i32 s36, s12, 11
	s_cmp_eq_u32 s36, s14
	s_cbranch_scc1 .LBB0_833
	s_mul_i32 s12, s36, 0x1800
	s_ashr_i32 s13, s12, 31
	s_lshl_b64 s[12:13], s[12:13], 2
	s_add_u32 s14, s20, s12
	s_addc_u32 s15, s21, s13
	s_add_u32 s12, s14, 0x203000
	s_addc_u32 s13, s15, 0
	s_add_u32 s14, s14, 0x204000
	s_addc_u32 s15, s15, 0
	v_lshl_add_u64 v[4:5], s[14:15], 0, v[32:33]
	v_lshl_add_u64 v[12:13], s[14:15], 0, v[36:37]
	v_lshl_add_u64 v[20:21], s[14:15], 0, v[38:39]
	v_lshl_add_u64 v[28:29], s[14:15], 0, v[40:41]
	global_load_dwordx4 v[4:7], v[4:5], off
	s_nop 0
	global_load_dwordx4 v[12:15], v[12:13], off
	s_nop 0
	global_load_dwordx4 v[20:23], v[20:21], off
	s_nop 0
	global_load_dwordx4 v[28:31], v[28:29], off
	s_nop 0
	global_load_dwordx4 v[0:3], v[44:45], off
	s_nop 0
	global_load_dwordx4 v[8:11], v[44:45], off offset:1024
	s_nop 0
	global_load_dwordx4 v[16:19], v[44:45], off offset:2048
	s_nop 0
	global_load_dwordx4 v[24:27], v[44:45], off offset:3072
	s_mov_b32 s14, s36
	s_waitcnt vmcnt(0)
	v_pk_add_f32 v[4:5], v[4:5], 1.0 op_sel_hi:[1,0]
	v_pk_add_f32 v[6:7], v[6:7], 1.0 op_sel_hi:[1,0]
	v_pk_add_f32 v[12:13], v[12:13], 1.0 op_sel_hi:[1,0]
	v_pk_add_f32 v[14:15], v[14:15], 1.0 op_sel_hi:[1,0]
	v_pk_add_f32 v[20:21], v[20:21], 1.0 op_sel_hi:[1,0]
	v_pk_add_f32 v[22:23], v[22:23], 1.0 op_sel_hi:[1,0]
	v_pk_add_f32 v[28:29], v[28:29], 1.0 op_sel_hi:[1,0]
	v_pk_add_f32 v[30:31], v[30:31], 1.0 op_sel_hi:[1,0]
	v_pk_mul_f32 v[0:1], v[0:1], v[4:5]
	v_pk_mul_f32 v[2:3], v[2:3], v[6:7]
	v_pk_mul_f32 v[8:9], v[8:9], v[12:13]
	v_pk_mul_f32 v[10:11], v[10:11], v[14:15]
	v_pk_mul_f32 v[16:17], v[16:17], v[20:21]
	v_pk_mul_f32 v[18:19], v[18:19], v[22:23]
	v_pk_mul_f32 v[24:25], v[24:25], v[28:29]
	v_pk_mul_f32 v[26:27], v[26:27], v[30:31]
	v_lshl_add_u64 v[4:5], s[12:13], 0, v[32:33]
	v_lshl_add_u64 v[12:13], s[12:13], 0, v[36:37]
	v_lshl_add_u64 v[20:21], s[12:13], 0, v[38:39]
	v_lshl_add_u64 v[28:29], s[12:13], 0, v[40:41]
	global_load_dwordx4 v[4:7], v[4:5], off
	s_nop 0
	global_load_dwordx4 v[12:15], v[12:13], off
	s_nop 0
	global_load_dwordx4 v[20:23], v[20:21], off
	s_nop 0
	global_load_dwordx4 v[28:31], v[28:29], off
	s_waitcnt vmcnt(1)
